# cmp pass 1: running max and sum updated in place (eight loop-carried copies per item gone), zero-adds dropped; cmp item DMA uses the scalar-base address form
# baseline (speedup 1.0000x reference)
; #define LAS __attribute__((address_space(3)))
; template <class G> __device__ __forceinline__ float gs_inv(const G& g) { float l = xsum32(xsum16(g.l)); return l > 0.f ? 1.f / l : 0.f; }
; #define RING_BARRIER() do { asm volatile("s_waitcnt lgkmcnt(0)" ::: "memory"); __builtin_amdgcn_s_barrier(); asm volatile("" ::: "memory"); } while (0)
; __device__ __forceinline__ void cmp_phase(Frame& F) {
;     ...
;         for (int i = 0; i < nit; ++i) { const int kt = i < nkt ? i : i - nkt;
;             asm volatile("s_waitcnt vmcnt(0)" ::: "memory"); RING_BARRIER();
;             if (i + 1 < nit) { const int kn = (i + 1 < nkt) ? i + 1 : i + 1 - nkt; ring8_dma(RL, Kb + (size_t)kn * 8192, Vb + (size_t)kn * 16384, F.lds + ((i + 1) & 1) * SLOT8, F.wave); }
;             LAS unsigned char* sb = F.lds + (i & 1) * SLOT8;
;             if (i == nkt) { i0 = gs_inv(g0); i1 = gs_inv(g1); }
;             const bool p1 = i < nkt; const float r0 = p1 ? smc_ref(g0) : g0.m - __builtin_amdgcn_logf(i0), r1 = p1 ? smc_ref(g1) : g1.m - __builtin_amdgcn_logf(i1);
;             f32x4 s0[4], s1[4];
;             qk8_tile2(s0, s1, g0, g1, sb + klane, -r0, -r1);
;             if (kt * 64 + 63 > ((t0 - 31) >> 4)) { mask_scores(s0, limA, 0x40000000u, kt * 64, kq); mask_scores(s1, limB, 0x40000000u, kt * 64, kq); }
;             if (i < nkt) { online_smc<false>(s0, g0, r0); online_smc<false>(s1, g1, r1); }
.LBB0_1570:
	s_sub_i32 s59, s59, 64
	s_add_i32 s79, s79, 64
	s_and_b64 vcc, exec, s[54:55]
	s_cbranch_vccnz .LBB0_1603

; #define LAS __attribute__((address_space(3)))
; #define RING_BARRIER() do { asm volatile("s_waitcnt lgkmcnt(0)" ::: "memory"); __builtin_amdgcn_s_barrier(); asm volatile("" ::: "memory"); } while (0)
; __device__ __forceinline__ void ring8_dma(const Ring8Lane& R, const char* K8p, const char* Vp, LAS unsigned char* sb, int wave) {
;     __builtin_amdgcn_global_load_lds((const unsigned*)(K8p + R.so[0]), (LAS unsigned*)(sb + wave * 1024), 16, 0, 0);
;     __builtin_amdgcn_global_load_lds((const unsigned*)((wave == 0 ? K8p : Vp) + R.so[1]), (LAS unsigned*)(sb + (wave + 8) * 1024), 16, 0, 0);
;     __builtin_amdgcn_global_load_lds((const unsigned*)(Vp + R.so[2]), (LAS unsigned*)(sb + (wave + 16) * 1024), 16, 0, 0);
;     if (wave <= 2) __builtin_amdgcn_global_load_lds((const unsigned*)(Vp + R.so[3]), (LAS unsigned*)(sb + (wave + 24) * 1024), 16, 0, 0);
; }
; __device__ __forceinline__ void cmp_phase(Frame& F) {
;     ...
;             asm volatile("s_waitcnt vmcnt(0)" ::: "memory"); RING_BARRIER();
;             if (i + 1 < nit) { const int kn = (i + 1 < nkt) ? i + 1 : i + 1 - nkt; ring8_dma(RL, Kb + (size_t)kn * 8192, Vb + (size_t)kn * 16384, F.lds + ((i + 1) & 1) * SLOT8, F.wave); }
.LBB0_1572:
	s_waitcnt vmcnt(0)
	s_add_i32 s36, s80, 1
	s_waitcnt lgkmcnt(0)
	s_barrier
	s_cmp_ge_u32 s36, s74
	s_cselect_b64 s[54:55], -1, 0
	s_and_b64 vcc, exec, s[54:55]
	s_cbranch_vccnz .LBB0_1575
	s_add_i32 s22, s76, s80
	s_cmp_lt_u32 s80, s60
	s_cselect_b32 s48, s36, s22
	s_lshl_b64 s[22:23], s[48:49], 13
	s_add_u32 s56, s24, s22
	s_addc_u32 s57, s25, s23
	s_lshl_b64 s[22:23], s[48:49], 14
	s_add_u32 s22, s52, s22
	s_addc_u32 s23, s53, s23
	s_bitcmp1_b32 s36, 0
	s_cselect_b32 s37, 0x6c00, 0
	s_add_i32 s37, s65, s37
	s_mov_b32 m0, s37
	s_and_b64 s[82:83], exec, s[44:45]
	global_load_lds_dwordx4 v114, s[56:57]
	s_cselect_b32 s57, s57, s23
	s_cselect_b32 s56, s56, s22
	s_add_i32 m0, s37, 0x2000
	s_and_b64 vcc, exec, s[18:19]
	global_load_lds_dwordx4 v122, s[56:57]
	s_add_i32 m0, s37, 0x4000
	s_nop 0
	global_load_lds_dwordx4 v120, s[22:23]
	s_cbranch_vccnz .LBB0_1575
	s_add_i32 m0, s37, 0x6000
	s_nop 0
	global_load_lds_dwordx4 v124, s[22:23]

; __device__ __forceinline__ float xmax16(float v) { float a = v, b = v; PL_SWAP16(a, b); return fmaxf(a, b); }
; __device__ __forceinline__ float xmax32(float v) { float a = v, b = v; PL_SWAP32(a, b); return fmaxf(a, b); }
; template <bool WITH_O, class G> __device__ __forceinline__ void online_smc(f32x4 (&s)[4], G& g, const float ref) {
;     float mx = s[0][0];
; #pragma unroll
;     for (int T_ = 0; T_ < 4; ++T_)
; #pragma unroll
;         for (int i = 0; i < 4; ++i) mx = fmaxf(mx, s[T_][i]);
;     const float t = mx + ref;
;     if (!__all(t <= g.m + SM_THR)) {
;         const float mr = xmax32(xmax16(t));
;         const float mn = fmaxf(g.m, mr); const float al = __builtin_amdgcn_exp2f(g.m - mn); g.m = mn; g.l *= al;
;         if (WITH_O) {
; #pragma unroll
;             for (int dt = 0; dt < 8; ++dt) g.o[dt] = g.o[dt] * al; }
;         const float d = ref - mn;
; #pragma unroll
;         for (int T_ = 0; T_ < 4; ++T_)
; #pragma unroll
;             for (int i = 0; i < 4; ++i) s[T_][i] += d;
;     }
;     float ps = 0.f;
; #pragma unroll
;     for (int T_ = 0; T_ < 4; ++T_)
; #pragma unroll
;         for (int i = 0; i < 4; ++i) { s[T_][i] = __builtin_amdgcn_exp2f(s[T_][i]); ps += s[T_][i]; }
;     g.l += ps;
.LBB0_1579:
	s_mov_b64 s[22:23], -1
	s_and_b64 vcc, exec, s[56:57]
	s_cbranch_vccz .LBB0_1585
	v_add_f32_e32 v159, v141, v135
	v_max_f32_e32 v134, v108, v109
	v_max3_f32 v134, v134, v110, v111
	v_max3_f32 v134, v134, v104, v105
	v_max3_f32 v134, v134, v106, v107
	v_max3_f32 v134, v134, v100, v101
	v_max3_f32 v134, v134, v102, v103
	v_max3_f32 v134, v134, v96, v97
	v_max3_f32 v134, v134, v98, v99
	v_add_f32_e32 v158, v140, v134
	v_cmp_le_f32_e32 vcc, v158, v159
	s_cmp_eq_u64 vcc, exec
	s_cbranch_scc1 .LBB0_1582
	v_mov_b32_e32 v134, v158
	s_nop 1
	v_permlane16_swap_b32 v158, v134
	v_max_f32_e32 v134, v134, v134
	v_max_f32_e32 v144, v158, v158
	v_max_f32_e32 v134, v144, v134
	v_mov_b32_e32 v144, v134
	s_nop 1
	v_permlane32_swap_b32 v134, v144
	v_max3_f32 v194, v141, v134, v144
	v_sub_f32_e32 v134, v141, v194
	v_exp_f32_e32 v134, v134
	v_sub_f32_e32 v144, v140, v194
	v_mul_f32_e32 v191, v191, v134
	v_mov_b32_e32 v141, v194
	v_add_f32_e32 v96, v96, v144
	v_add_f32_e32 v97, v97, v144
	v_add_f32_e32 v98, v98, v144
	v_add_f32_e32 v99, v99, v144
	v_add_f32_e32 v100, v100, v144
	v_add_f32_e32 v101, v101, v144
	v_add_f32_e32 v102, v102, v144
	v_add_f32_e32 v103, v103, v144
	v_add_f32_e32 v104, v104, v144
	v_add_f32_e32 v105, v105, v144
	v_add_f32_e32 v106, v106, v144
	v_add_f32_e32 v107, v107, v144
	v_add_f32_e32 v108, v108, v144
	v_add_f32_e32 v109, v109, v144
	v_add_f32_e32 v110, v110, v144
	v_add_f32_e32 v111, v111, v144
.LBB0_1582:
	v_max_f32_e32 v134, v88, v89
	v_max3_f32 v134, v134, v90, v91
	v_max3_f32 v134, v134, v84, v85
	v_max3_f32 v134, v134, v86, v87
	v_max3_f32 v134, v134, v80, v81
	v_max3_f32 v134, v134, v82, v83
	v_max3_f32 v134, v134, v92, v93
	v_max3_f32 v134, v134, v94, v95
	v_pk_add_f32 v[170:171], v[138:139], v[134:135]
	v_cmp_le_f32_e32 vcc, v170, v171
	s_cmp_eq_u64 vcc, exec
	s_cbranch_scc1 .LBB0_1584
	v_mov_b32_e32 v134, v170
	s_nop 1
	v_permlane16_swap_b32 v170, v134
	v_max_f32_e32 v134, v134, v134
	v_max_f32_e32 v140, v170, v170
	v_max_f32_e32 v134, v140, v134
	v_mov_b32_e32 v140, v134
	s_nop 1
	v_permlane32_swap_b32 v134, v140
	v_max3_f32 v134, v139, v134, v140
	v_sub_f32_e32 v140, v139, v134
	v_exp_f32_e32 v140, v140
	v_sub_f32_e32 v138, v138, v134
	v_mul_f32_e32 v190, v190, v140
	v_mov_b32_e32 v139, v134
	v_add_f32_e32 v80, v80, v138
	v_add_f32_e32 v81, v81, v138
	v_add_f32_e32 v82, v82, v138
	v_add_f32_e32 v83, v83, v138
	v_add_f32_e32 v84, v84, v138
	v_add_f32_e32 v85, v85, v138
	v_add_f32_e32 v86, v86, v138
	v_add_f32_e32 v87, v87, v138
	v_add_f32_e32 v88, v88, v138
	v_add_f32_e32 v89, v89, v138
	v_add_f32_e32 v90, v90, v138
	v_add_f32_e32 v91, v91, v138
	v_add_f32_e32 v92, v92, v138
	v_add_f32_e32 v93, v93, v138
	v_add_f32_e32 v94, v94, v138
	v_add_f32_e32 v95, v95, v138
.LBB0_1584:
	v_exp_f32_e32 v138, v108
	v_exp_f32_e32 v150, v109
	v_exp_f32_e32 v151, v110
	v_exp_f32_e32 v156, v111
	v_add_f32_e32 v138, v138, v150
	v_exp_f32_e32 v150, v104
	v_add_f32_e32 v138, v151, v138
	v_exp_f32_e32 v151, v105
	v_exp_f32_e32 v152, v106
	v_add_f32_e32 v138, v156, v138
	v_exp_f32_e32 v153, v107
	v_add_f32_e32 v138, v150, v138
	v_exp_f32_e32 v150, v100
	v_add_f32_e32 v138, v151, v138
	v_exp_f32_e32 v148, v101
	v_add_f32_e32 v138, v152, v138
	v_exp_f32_e32 v149, v102
	v_add_f32_e32 v138, v153, v138
	v_exp_f32_e32 v151, v103
	v_add_f32_e32 v138, v150, v138
	v_exp_f32_e32 v144, v96
	v_add_f32_e32 v138, v148, v138
	v_exp_f32_e32 v145, v97
	v_add_f32_e32 v138, v149, v138
	v_exp_f32_e32 v146, v98
	v_add_f32_e32 v138, v151, v138
	v_exp_f32_e32 v147, v99
	v_add_f32_e32 v138, v144, v138
	v_add_f32_e32 v138, v145, v138
	v_add_f32_e32 v138, v146, v138
	v_add_f32_e32 v138, v147, v138
	v_add_f32_e32 v191, v191, v138
	v_exp_f32_e32 v138, v88
	v_exp_f32_e32 v145, v89
	v_exp_f32_e32 v146, v90
	v_exp_f32_e32 v147, v91
	v_add_f32_e32 v138, v138, v145
	v_exp_f32_e32 v145, v84
	v_add_f32_e32 v138, v146, v138
	v_exp_f32_e32 v146, v85
	v_add_f32_e32 v138, v147, v138
	v_exp_f32_e32 v147, v86
	v_exp_f32_e32 v148, v87
	v_add_f32_e32 v138, v145, v138
	v_exp_f32_e32 v145, v80
	v_add_f32_e32 v138, v146, v138
	v_exp_f32_e32 v146, v81
	v_add_f32_e32 v138, v147, v138
	v_exp_f32_e32 v147, v82
	v_add_f32_e32 v138, v148, v138
	v_exp_f32_e32 v148, v83
	v_add_f32_e32 v138, v145, v138
	v_exp_f32_e32 v145, v92
	v_add_f32_e32 v138, v146, v138
	v_exp_f32_e32 v146, v93
	v_add_f32_e32 v138, v147, v138
	v_exp_f32_e32 v147, v94
	v_add_f32_e32 v138, v148, v138
	v_exp_f32_e32 v148, v95
	v_add_f32_e32 v138, v145, v138
	v_add_f32_e32 v138, v146, v138
	v_add_f32_e32 v138, v147, v138
	v_add_f32_e32 v138, v148, v138
	v_add_f32_e32 v190, v190, v138
	s_branch .LBB0_1570
